# attention query columns also written in MFMA-fragment order (inside the token-major rows' now unused retention q/k span); attention task query fragment loads lane-contiguous
# baseline (speedup 1.0000x reference)
;     __device__ __forceinline__ void operator()(const f32x4 (&acc)[2][2][4][2], const Unit& u, int wr, int wc, int fr, int fq) const {
;         const int row0 = u.pm * BM + wr * 64 + fr, kind = u.pn >> 2;
; #pragma unroll
;         for (int ai = 0; ai < 2; ++ai)
; #pragma unroll
;             for (int m = 0; m < 4; ++m) {
;                 const int row = row0 + ai * HALF + m * 16, pos = row & (MS - 1);
;                 const float rs = rstd[row];
; #pragma unroll
;                 for (int bj = 0; bj < 2; ++bj) {
;                     const int c0 = u.pn * BM + bj * HALF + wc * 32 + 8 * fq;
;                     f32x4 v0 = acc[ai][bj][m][0] * rs, v1 = acc[ai][bj][m][1] * rs;
;                     if (kind <= 1) {
;                         float s = (v0[0] * v0[0] + v0[1] * v0[1]) + (v0[2] * v0[2] + v0[3] * v0[3]) + (v1[0] * v1[0] + v1[1] * v1[1]) + (v1[2] * v1[2] + v1[3] * v1[3]);
;                         s += __shfl_xor(s, 16); s += __shfl_xor(s, 32);
;                         const int head = (u.pn & 3) * 2 + bj;
;                         if (fq == 0) ssq[(size_t)((kind * 8 + head) * 4 + wc) * MT + row] = s;
;                     } else if (kind <= 3) {
;                         const int i0 = (c0 & 127) >> 1;
;                         const f32x4 csa = *(const f32x4*)(cs + (size_t)pos * 64 + i0), csb = *(const f32x4*)(cs + (size_t)pos * 64 + i0 + 2);
;                         const float sc = (kind == 3) ? KSCALE : 1.0f;
;                         f32x4 w0, w1;
;                         w0[0] = (v0[0] * csa[0] - v0[1] * csa[1]) * sc; w0[1] = (v0[1] * csa[0] + v0[0] * csa[1]) * sc;
;                         w0[2] = (v0[2] * csa[2] - v0[3] * csa[3]) * sc; w0[3] = (v0[3] * csa[2] + v0[2] * csa[3]) * sc;
;                         w1[0] = (v1[0] * csb[0] - v1[1] * csb[1]) * sc; w1[1] = (v1[1] * csb[0] + v1[0] * csb[1]) * sc;
;                         w1[2] = (v1[2] * csb[2] - v1[3] * csb[3]) * sc; w1[3] = (v1[3] * csb[2] + v1[2] * csb[3]) * sc;
;                         v0 = w0; v1 = w1;
;                     } else {
; #pragma unroll
;                         for (int j = 0; j < 4; ++j) { v0[j] = v0[j] * __builtin_amdgcn_rcpf(1.0f + __builtin_amdgcn_exp2f(-1.4426950408889634f * v0[j]));
;                                                       v1[j] = v1[j] * __builtin_amdgcn_rcpf(1.0f + __builtin_amdgcn_exp2f(-1.4426950408889634f * v1[j])); }
.LBB0_226:
	v_mov_b32_e32 v240, s66
	v_add_u32_e32 v245, -16, v240
	v_mov_b32_e32 v241, 0x2ec00000
	v_mov_b32_e32 v233, 0x800
	v_mov_b32_e32 v246, 0x2000
	v_mov_b32_e32 v242, 0x1000
	v_cmp_gt_u32_e64 s[100:101], 16, v240
	v_add_u32_e32 v247, -8, v240
	v_mov_b32_e32 v248, 0xe000000
	v_mov_b32_e32 v249, 0x1000
	s_nop 0
	v_cndmask_b32_e64 v245, v245, v247, s[100:101]
	v_cndmask_b32_e64 v241, v241, v248, s[100:101]
	v_cndmask_b32_e64 v233, v233, v249, s[100:101]
	v_cmp_gt_u32_e64 s[100:101], 8, v240
	v_mov_b32_e32 v248, 0x12001000
	v_mov_b32_e32 v249, 0x2900
	v_mov_b32_e32 v247, 0x5200
	s_nop 0
	v_cndmask_b32_e64 v245, v245, v240, s[100:101]
	v_cndmask_b32_e64 v241, v241, v248, s[100:101]
	v_cndmask_b32_e64 v233, v233, v249, s[100:101]
	v_cndmask_b32_e64 v246, v246, v247, s[100:101]
	v_cndmask_b32_e64 v242, v242, v249, s[100:101]
	v_cmp_gt_u32_e64 s[100:101], 4, v240
	s_nop 1
	v_cndmask_b32_e64 v247, 0, 1, s[100:101]
	v_cmp_lt_u32_e64 s[100:101], 7, v240
	s_nop 1
	v_cndmask_b32_e64 v248, 0, 1, s[100:101]
	v_or_b32_e32 v247, v247, v248
	v_cmp_ne_u32_e64 s[100:101], 0, v247
	v_mul_lo_u32 v240, v245, v246
	v_lshl_add_u32 v240, v161, 5, v240
	v_and_b32_e32 v245, 15, v159
	v_lshl_add_u32 v240, v245, 4, v240
	v_add_u32_e32 v240, v241, v240
	v_mov_b32_e32 v241, 0
	v_mov_b32_e32 v238, s62
	v_mov_b32_e32 v239, s63
	v_lshl_add_u64 v[238:239], v[238:239], 0, v[240:241]
	v_mov_b32_e32 v244, 0x100
	s_nop 0
	v_cndmask_b32_e64 v242, v244, v242, s[100:101]
	v_mov_b32_e32 v243, 0
	v_lshl_add_u32 v142, s38, 8, v159
	v_readlane_b32 s56, v250, 22
	v_ashrrev_i32_e32 v143, 31, v142
	v_readlane_b32 s57, v250, 23
	s_ashr_i32 s4, s66, 2
	s_cmp_gt_i32 s4, 1
	v_lshl_add_u64 v[146:147], v[142:143], 2, s[56:57]
	global_load_dword v148, v[146:147], off
	global_load_dword v226, v[146:147], off offset:64
	global_load_dword v227, v[146:147], off offset:128
	global_load_dword v228, v[146:147], off offset:192
	global_load_dword v229, v[146:147], off offset:512
	global_load_dword v230, v[146:147], off offset:576
	global_load_dword v231, v[146:147], off offset:640
	global_load_dword v232, v[146:147], off offset:704
	s_cselect_b64 s[0:1], -1, 0
	s_cmp_gt_u32 s4, 3
	s_cselect_b64 s[8:9], -1, 0
	s_cmp_eq_u32 s4, 3
	v_lshlrev_b32_e32 v149, 6, v142
	s_cselect_b64 vcc, -1, 0
	v_and_b32_e32 v163, 0x1f3c0, v149
	v_cndmask_b32_e32 v144, 1.0, v220, vcc
	s_mov_b64 s[2:3], -1
	s_and_b64 vcc, exec, s[0:1]
	s_waitcnt vmcnt(0)
	v_pk_mul_f32 v[126:127], v[126:127], v[148:149] op_sel_hi:[1,0]
	v_pk_mul_f32 v[124:125], v[124:125], v[148:149] op_sel_hi:[1,0]
	v_pk_mul_f32 v[122:123], v[122:123], v[148:149] op_sel_hi:[1,0]
	v_pk_mul_f32 v[120:121], v[120:121], v[148:149] op_sel_hi:[1,0]
	v_cndmask_b32_e64 v149, 0, 1, s[8:9]
	v_cmp_ne_u32_e64 s[38:39], 1, v149
	s_cbranch_vccz .LBB0_232
	s_and_b64 vcc, exec, s[38:39]
	s_cbranch_vccnz .LBB0_229
	v_mul_f32_e32 v149, 0xbfb8aa3b, v124
	v_exp_f32_e32 v149, v149
	v_mul_f32_e32 v150, 0xbfb8aa3b, v120
	v_mul_f32_e32 v151, 0xbfb8aa3b, v125
	v_exp_f32_e32 v152, v150
	v_exp_f32_e32 v151, v151
	v_add_f32_e32 v149, 1.0, v149
	v_rcp_f32_e32 v150, v149
	v_add_f32_e32 v149, 1.0, v152
	v_rcp_f32_e32 v154, v149
	v_add_f32_e32 v149, 1.0, v151
	v_mul_f32_e32 v153, 0xbfb8aa3b, v122
	v_rcp_f32_e32 v151, v149
	v_mul_f32_e32 v149, 0xbfb8aa3b, v121
	v_mul_f32_e32 v152, 0xbfb8aa3b, v126
	v_exp_f32_e32 v153, v153
	v_mul_f32_e32 v155, 0xbfb8aa3b, v127
	v_mul_f32_e32 v156, 0xbfb8aa3b, v123
	v_exp_f32_e32 v149, v149
	v_exp_f32_e32 v152, v152
	v_exp_f32_e32 v155, v155
	v_exp_f32_e32 v157, v156
	v_add_f32_e32 v153, 1.0, v153
	v_add_f32_e32 v149, 1.0, v149
	v_add_f32_e32 v152, 1.0, v152
	v_rcp_f32_e32 v156, v153
	v_add_f32_e32 v153, 1.0, v155
	v_add_f32_e32 v155, 1.0, v157
	v_rcp_f32_e32 v152, v152
	v_rcp_f32_e32 v153, v153
	v_rcp_f32_e32 v157, v155
	v_rcp_f32_e32 v155, v149
	v_pk_mul_f32 v[150:151], v[124:125], v[150:151]
	v_pk_mul_f32 v[152:153], v[126:127], v[152:153]
	v_pk_mul_f32 v[156:157], v[122:123], v[156:157]
	v_pk_mul_f32 v[154:155], v[120:121], v[154:155]
	s_mov_b64 s[2:3], 0

;     __device__ __forceinline__ void operator()(const f32x4 (&acc)[2][2][4][2], const Unit& u, int wr, int wc, int fr, int fq) const {
;     ...
;                 for (int bj = 0; bj < 2; ++bj) {
;                     const int c0 = u.pn * BM + bj * HALF + wc * 32 + 8 * fq;
;                     f32x4 v0 = acc[ai][bj][m][0] * rs, v1 = acc[ai][bj][m][1] * rs;
;                     if (kind <= 1) {
;                         float s = (v0[0] * v0[0] + v0[1] * v0[1]) + (v0[2] * v0[2] + v0[3] * v0[3]) + (v1[0] * v1[0] + v1[1] * v1[1]) + (v1[2] * v1[2] + v1[3] * v1[3]);
;                         s += __shfl_xor(s, 16); s += __shfl_xor(s, 32);
;                         const int head = (u.pn & 3) * 2 + bj;
;                         if (fq == 0) ssq[(size_t)((kind * 8 + head) * 4 + wc) * MT + row] = s;
;                     } else if (kind <= 3) {
;                         const int i0 = (c0 & 127) >> 1;
;                         const f32x4 csa = *(const f32x4*)(cs + (size_t)pos * 64 + i0), csb = *(const f32x4*)(cs + (size_t)pos * 64 + i0 + 2);
;                         const float sc = (kind == 3) ? KSCALE : 1.0f;
;                         f32x4 w0, w1;
;                         w0[0] = (v0[0] * csa[0] - v0[1] * csa[1]) * sc; w0[1] = (v0[1] * csa[0] + v0[0] * csa[1]) * sc;
;                         w0[2] = (v0[2] * csa[2] - v0[3] * csa[3]) * sc; w0[3] = (v0[3] * csa[2] + v0[2] * csa[3]) * sc;
;                         w1[0] = (v1[0] * csb[0] - v1[1] * csb[1]) * sc; w1[1] = (v1[1] * csb[0] + v1[0] * csb[1]) * sc;
;                         w1[2] = (v1[2] * csb[2] - v1[3] * csb[3]) * sc; w1[3] = (v1[3] * csb[2] + v1[2] * csb[3]) * sc;
;                         v0 = w0; v1 = w1;
;                     } else {
; #pragma unroll
;                         for (int j = 0; j < 4; ++j) { v0[j] = v0[j] * __builtin_amdgcn_rcpf(1.0f + __builtin_amdgcn_exp2f(-1.4426950408889634f * v0[j]));
;                                                       v1[j] = v1[j] * __builtin_amdgcn_rcpf(1.0f + __builtin_amdgcn_exp2f(-1.4426950408889634f * v1[j])); }
;                     }
;                     u32x4 w; w.x = cvt_pk_bf16(v0[0], v0[1]); w.y = cvt_pk_bf16(v0[2], v0[3]); w.z = cvt_pk_bf16(v1[0], v1[1]); w.w = cvt_pk_bf16(v1[2], v1[3]);
;                     *(u32x4*)(O + (size_t)row * TOKP + c0) = w;
.LBB0_236:
	v_lshl_or_b32 v120, s66, 8, v161
	v_mov_b64_e32 v[122:123], s[80:81]
	s_movk_i32 s2, 0x2900
	v_mad_i64_i32 v[122:123], s[2:3], v142, s2, v[122:123]
	v_ashrrev_i32_e32 v121, 31, v120
	v_cvt_pk_bf16_f32 v124, v150, v151
	v_cvt_pk_bf16_f32 v125, v152, v153
	v_lshl_add_u64 v[122:123], v[120:121], 1, v[122:123]
	v_cvt_pk_bf16_f32 v126, v154, v155
	v_cvt_pk_bf16_f32 v127, v156, v157
	v_and_b32_e32 v244, -16, v142
	v_mul_lo_u32 v244, v244, v233
	v_mov_b32_e32 v245, 0
	v_lshl_add_u64 v[246:247], v[244:245], 0, v[238:239]
	v_cndmask_b32_e64 v246, v122, v246, s[100:101]
	v_cndmask_b32_e64 v247, v123, v247, s[100:101]
	v_lshl_add_u64 v[248:249], v[246:247], 0, v[242:243]
	global_store_dwordx4 v[246:247], v[124:127], off
	v_mov_b32_e32 v149, v148
	v_pk_mul_f32 v[116:117], v[116:117], v[148:149]
	v_mov_b32_e32 v124, v148
	v_mov_b32_e32 v125, v148
	v_pk_mul_f32 v[118:119], v[118:119], v[124:125]
	v_pk_mul_f32 v[114:115], v[114:115], v[124:125]
	v_cndmask_b32_e64 v124, 0, 1, s[0:1]
	v_pk_mul_f32 v[112:113], v[112:113], v[148:149]
	v_cmp_ne_u32_e64 s[40:41], 1, v124
	s_andn2_b64 vcc, exec, s[0:1]
	s_mov_b64 s[0:1], -1
	s_cbranch_vccnz .LBB0_242
	s_and_b64 vcc, exec, s[38:39]
	s_cbranch_vccnz .LBB0_239
	v_mul_f32_e32 v125, 0xbfb8aa3b, v112
	v_mul_f32_e32 v126, 0xbfb8aa3b, v117
	v_exp_f32_e32 v125, v125
	v_exp_f32_e32 v126, v126
	v_mul_f32_e32 v127, 0xbfb8aa3b, v118
	v_mul_f32_e32 v149, 0xbfb8aa3b, v114
	v_add_f32_e32 v125, 1.0, v125
	v_rcp_f32_e32 v148, v125
	v_add_f32_e32 v125, 1.0, v126
	v_mul_f32_e32 v126, 0xbfb8aa3b, v113
	v_exp_f32_e32 v126, v126
	v_exp_f32_e32 v127, v127
	v_exp_f32_e32 v149, v149
	v_mul_f32_e32 v124, 0xbfb8aa3b, v116
	v_add_f32_e32 v152, 1.0, v126
	v_add_f32_e32 v126, 1.0, v127
	v_add_f32_e32 v127, 1.0, v149
	v_mul_f32_e32 v149, 0xbfb8aa3b, v119
	v_mul_f32_e32 v150, 0xbfb8aa3b, v115
	v_exp_f32_e32 v124, v124
	v_exp_f32_e32 v149, v149
	v_exp_f32_e32 v151, v150
	v_rcp_f32_e32 v150, v127
	v_add_f32_e32 v124, 1.0, v124
	v_add_f32_e32 v127, 1.0, v149
	v_add_f32_e32 v149, 1.0, v151
	v_rcp_f32_e32 v124, v124
	v_rcp_f32_e32 v125, v125
	v_rcp_f32_e32 v126, v126
	v_rcp_f32_e32 v127, v127
	v_rcp_f32_e32 v151, v149
	v_rcp_f32_e32 v149, v152
	v_pk_mul_f32 v[124:125], v[116:117], v[124:125]
	v_pk_mul_f32 v[126:127], v[118:119], v[126:127]
	v_pk_mul_f32 v[150:151], v[114:115], v[150:151]
	v_pk_mul_f32 v[148:149], v[112:113], v[148:149]
	s_mov_b64 s[0:1], 0

;     __device__ __forceinline__ void operator()(const f32x4 (&acc)[2][2][4][2], const Unit& u, int wr, int wc, int fr, int fq) const {
;     ...
;                 for (int bj = 0; bj < 2; ++bj) {
;                     const int c0 = u.pn * BM + bj * HALF + wc * 32 + 8 * fq;
;                     f32x4 v0 = acc[ai][bj][m][0] * rs, v1 = acc[ai][bj][m][1] * rs;
;                     if (kind <= 1) {
;                         float s = (v0[0] * v0[0] + v0[1] * v0[1]) + (v0[2] * v0[2] + v0[3] * v0[3]) + (v1[0] * v1[0] + v1[1] * v1[1]) + (v1[2] * v1[2] + v1[3] * v1[3]);
;                         s += __shfl_xor(s, 16); s += __shfl_xor(s, 32);
;                         const int head = (u.pn & 3) * 2 + bj;
;                         if (fq == 0) ssq[(size_t)((kind * 8 + head) * 4 + wc) * MT + row] = s;
;                     } else if (kind <= 3) {
;                         const int i0 = (c0 & 127) >> 1;
;                         const f32x4 csa = *(const f32x4*)(cs + (size_t)pos * 64 + i0), csb = *(const f32x4*)(cs + (size_t)pos * 64 + i0 + 2);
;                         const float sc = (kind == 3) ? KSCALE : 1.0f;
;                         f32x4 w0, w1;
;                         w0[0] = (v0[0] * csa[0] - v0[1] * csa[1]) * sc; w0[1] = (v0[1] * csa[0] + v0[0] * csa[1]) * sc;
;                         w0[2] = (v0[2] * csa[2] - v0[3] * csa[3]) * sc; w0[3] = (v0[3] * csa[2] + v0[2] * csa[3]) * sc;
;                         w1[0] = (v1[0] * csb[0] - v1[1] * csb[1]) * sc; w1[1] = (v1[1] * csb[0] + v1[0] * csb[1]) * sc;
;                         w1[2] = (v1[2] * csb[2] - v1[3] * csb[3]) * sc; w1[3] = (v1[3] * csb[2] + v1[2] * csb[3]) * sc;
;                         v0 = w0; v1 = w1;
;                     } else {
; #pragma unroll
;                         for (int j = 0; j < 4; ++j) { v0[j] = v0[j] * __builtin_amdgcn_rcpf(1.0f + __builtin_amdgcn_exp2f(-1.4426950408889634f * v0[j]));
;                                                       v1[j] = v1[j] * __builtin_amdgcn_rcpf(1.0f + __builtin_amdgcn_exp2f(-1.4426950408889634f * v1[j])); }
;                     }
;                     u32x4 w; w.x = cvt_pk_bf16(v0[0], v0[1]); w.y = cvt_pk_bf16(v0[2], v0[3]); w.z = cvt_pk_bf16(v1[0], v1[1]); w.w = cvt_pk_bf16(v1[2], v1[3]);
;                     *(u32x4*)(O + (size_t)row * TOKP + c0) = w;
.LBB0_256:
	v_mov_b64_e32 v[104:105], s[80:81]
	s_movk_i32 s0, 0x2900
	v_mad_i64_i32 v[104:105], s[0:1], v114, s0, v[104:105]
	v_cvt_pk_bf16_f32 v106, v116, v117
	v_cvt_pk_bf16_f32 v107, v118, v119
	v_lshl_add_u64 v[104:105], v[120:121], 1, v[104:105]
	v_mov_b32_e32 v113, v112
	v_cvt_pk_bf16_f32 v108, v122, v123
	v_cvt_pk_bf16_f32 v109, v124, v125
	v_and_b32_e32 v244, -16, v114
	v_mul_lo_u32 v244, v244, v233
	v_mov_b32_e32 v245, 0
	v_lshl_add_u64 v[246:247], v[244:245], 0, v[238:239]
	v_cndmask_b32_e64 v246, v104, v246, s[100:101]
	v_cndmask_b32_e64 v247, v105, v247, s[100:101]
	v_lshl_add_u64 v[248:249], v[246:247], 0, v[242:243]
	global_store_dwordx4 v[246:247], v[106:109], off
	v_pk_mul_f32 v[100:101], v[100:101], v[112:113]
	v_pk_mul_f32 v[96:97], v[96:97], v[112:113]
	v_mov_b32_e32 v106, v112
	v_mov_b32_e32 v107, v112
	v_pk_mul_f32 v[102:103], v[102:103], v[106:107]
	v_pk_mul_f32 v[98:99], v[98:99], v[106:107]
	s_and_b64 vcc, exec, s[40:41]
	s_mov_b64 s[0:1], -1
	s_cbranch_vccnz .LBB0_262
	s_and_b64 vcc, exec, s[38:39]
	s_cbranch_vccnz .LBB0_259
	v_mul_f32_e32 v107, 0xbfb8aa3b, v96
	v_mul_f32_e32 v108, 0xbfb8aa3b, v101
	v_exp_f32_e32 v107, v107
	v_exp_f32_e32 v108, v108
	v_mul_f32_e32 v109, 0xbfb8aa3b, v102
	v_mul_f32_e32 v111, 0xbfb8aa3b, v98
	v_add_f32_e32 v107, 1.0, v107
	v_rcp_f32_e32 v110, v107
	v_add_f32_e32 v107, 1.0, v108
	v_mul_f32_e32 v108, 0xbfb8aa3b, v97
	v_exp_f32_e32 v108, v108
	v_exp_f32_e32 v109, v109
	v_exp_f32_e32 v111, v111
	v_mul_f32_e32 v106, 0xbfb8aa3b, v100
	v_add_f32_e32 v114, 1.0, v108
	v_add_f32_e32 v108, 1.0, v109
	v_add_f32_e32 v109, 1.0, v111
	v_mul_f32_e32 v111, 0xbfb8aa3b, v103
	v_mul_f32_e32 v112, 0xbfb8aa3b, v99
	v_exp_f32_e32 v106, v106
	v_exp_f32_e32 v111, v111
	v_exp_f32_e32 v113, v112
	v_rcp_f32_e32 v112, v109
	v_add_f32_e32 v106, 1.0, v106
	v_add_f32_e32 v109, 1.0, v111
	v_add_f32_e32 v111, 1.0, v113
	v_rcp_f32_e32 v106, v106
	v_rcp_f32_e32 v107, v107
	v_rcp_f32_e32 v108, v108
	v_rcp_f32_e32 v109, v109
	v_rcp_f32_e32 v113, v111
	v_rcp_f32_e32 v111, v114
	v_pk_mul_f32 v[106:107], v[100:101], v[106:107]
	v_pk_mul_f32 v[108:109], v[102:103], v[108:109]
	v_pk_mul_f32 v[112:113], v[98:99], v[112:113]
	v_pk_mul_f32 v[110:111], v[96:97], v[110:111]
	s_mov_b64 s[0:1], 0

;     __device__ __forceinline__ void operator()(const f32x4 (&acc)[2][2][4][2], const Unit& u, int wr, int wc, int fr, int fq) const {
;     ...
;                 for (int bj = 0; bj < 2; ++bj) {
;                     const int c0 = u.pn * BM + bj * HALF + wc * 32 + 8 * fq;
;                     f32x4 v0 = acc[ai][bj][m][0] * rs, v1 = acc[ai][bj][m][1] * rs;
;                     if (kind <= 1) {
;                         float s = (v0[0] * v0[0] + v0[1] * v0[1]) + (v0[2] * v0[2] + v0[3] * v0[3]) + (v1[0] * v1[0] + v1[1] * v1[1]) + (v1[2] * v1[2] + v1[3] * v1[3]);
;                         s += __shfl_xor(s, 16); s += __shfl_xor(s, 32);
;                         const int head = (u.pn & 3) * 2 + bj;
;                         if (fq == 0) ssq[(size_t)((kind * 8 + head) * 4 + wc) * MT + row] = s;
;                     } else if (kind <= 3) {
;                         const int i0 = (c0 & 127) >> 1;
;                         const f32x4 csa = *(const f32x4*)(cs + (size_t)pos * 64 + i0), csb = *(const f32x4*)(cs + (size_t)pos * 64 + i0 + 2);
;                         const float sc = (kind == 3) ? KSCALE : 1.0f;
;                         f32x4 w0, w1;
;                         w0[0] = (v0[0] * csa[0] - v0[1] * csa[1]) * sc; w0[1] = (v0[1] * csa[0] + v0[0] * csa[1]) * sc;
;                         w0[2] = (v0[2] * csa[2] - v0[3] * csa[3]) * sc; w0[3] = (v0[3] * csa[2] + v0[2] * csa[3]) * sc;
;                         w1[0] = (v1[0] * csb[0] - v1[1] * csb[1]) * sc; w1[1] = (v1[1] * csb[0] + v1[0] * csb[1]) * sc;
;                         w1[2] = (v1[2] * csb[2] - v1[3] * csb[3]) * sc; w1[3] = (v1[3] * csb[2] + v1[2] * csb[3]) * sc;
;                         v0 = w0; v1 = w1;
;                     } else {
; #pragma unroll
;                         for (int j = 0; j < 4; ++j) { v0[j] = v0[j] * __builtin_amdgcn_rcpf(1.0f + __builtin_amdgcn_exp2f(-1.4426950408889634f * v0[j]));
;                                                       v1[j] = v1[j] * __builtin_amdgcn_rcpf(1.0f + __builtin_amdgcn_exp2f(-1.4426950408889634f * v1[j])); }
;                     }
;                     u32x4 w; w.x = cvt_pk_bf16(v0[0], v0[1]); w.y = cvt_pk_bf16(v0[2], v0[3]); w.z = cvt_pk_bf16(v1[0], v1[1]); w.w = cvt_pk_bf16(v1[2], v1[3]);
;                     *(u32x4*)(O + (size_t)row * TOKP + c0) = w;
.LBB0_276:
	v_mov_b64_e32 v[88:89], s[80:81]
	s_movk_i32 s0, 0x2900
	v_mad_i64_i32 v[88:89], s[0:1], v98, s0, v[88:89]
	v_cvt_pk_bf16_f32 v90, v100, v101
	v_cvt_pk_bf16_f32 v91, v102, v103
	v_lshl_add_u64 v[88:89], v[120:121], 1, v[88:89]
	v_mov_b32_e32 v97, v96
	v_cvt_pk_bf16_f32 v92, v104, v105
	v_cvt_pk_bf16_f32 v93, v106, v107
	v_and_b32_e32 v244, -16, v98
	v_mul_lo_u32 v244, v244, v233
	v_mov_b32_e32 v245, 0
	v_lshl_add_u64 v[246:247], v[244:245], 0, v[238:239]
	v_cndmask_b32_e64 v246, v88, v246, s[100:101]
	v_cndmask_b32_e64 v247, v89, v247, s[100:101]
	v_lshl_add_u64 v[248:249], v[246:247], 0, v[242:243]
	global_store_dwordx4 v[246:247], v[90:93], off
	v_pk_mul_f32 v[84:85], v[84:85], v[96:97]
	v_pk_mul_f32 v[80:81], v[80:81], v[96:97]
	v_mov_b32_e32 v90, v96
	v_mov_b32_e32 v91, v96
	v_pk_mul_f32 v[86:87], v[86:87], v[90:91]
	v_pk_mul_f32 v[82:83], v[82:83], v[90:91]
	s_and_b64 vcc, exec, s[40:41]
	s_mov_b64 s[0:1], -1
	s_cbranch_vccnz .LBB0_282
	s_and_b64 vcc, exec, s[38:39]
	s_cbranch_vccnz .LBB0_279
	v_mul_f32_e32 v91, 0xbfb8aa3b, v80
	v_mul_f32_e32 v92, 0xbfb8aa3b, v85
	v_exp_f32_e32 v91, v91
	v_exp_f32_e32 v92, v92
	v_mul_f32_e32 v93, 0xbfb8aa3b, v86
	v_mul_f32_e32 v95, 0xbfb8aa3b, v82
	v_add_f32_e32 v91, 1.0, v91
	v_rcp_f32_e32 v94, v91
	v_add_f32_e32 v91, 1.0, v92
	v_mul_f32_e32 v92, 0xbfb8aa3b, v81
	v_exp_f32_e32 v92, v92
	v_exp_f32_e32 v93, v93
	v_exp_f32_e32 v95, v95
	v_mul_f32_e32 v90, 0xbfb8aa3b, v84
	v_add_f32_e32 v98, 1.0, v92
	v_add_f32_e32 v92, 1.0, v93
	v_add_f32_e32 v93, 1.0, v95
	v_mul_f32_e32 v95, 0xbfb8aa3b, v87
	v_mul_f32_e32 v96, 0xbfb8aa3b, v83
	v_exp_f32_e32 v90, v90
	v_exp_f32_e32 v95, v95
	v_exp_f32_e32 v97, v96
	v_rcp_f32_e32 v96, v93
	v_add_f32_e32 v90, 1.0, v90
	v_add_f32_e32 v93, 1.0, v95
	v_add_f32_e32 v95, 1.0, v97
	v_rcp_f32_e32 v90, v90
	v_rcp_f32_e32 v91, v91
	v_rcp_f32_e32 v92, v92
	v_rcp_f32_e32 v93, v93
	v_rcp_f32_e32 v97, v95
	v_rcp_f32_e32 v95, v98
	v_pk_mul_f32 v[90:91], v[84:85], v[90:91]
	v_pk_mul_f32 v[92:93], v[86:87], v[92:93]
	v_pk_mul_f32 v[96:97], v[82:83], v[96:97]
	v_pk_mul_f32 v[94:95], v[80:81], v[94:95]
	s_mov_b64 s[0:1], 0

;     __device__ __forceinline__ void operator()(const f32x4 (&acc)[2][2][4][2], const Unit& u, int wr, int wc, int fr, int fq) const {
;     ...
;                 for (int bj = 0; bj < 2; ++bj) {
;                     const int c0 = u.pn * BM + bj * HALF + wc * 32 + 8 * fq;
;                     f32x4 v0 = acc[ai][bj][m][0] * rs, v1 = acc[ai][bj][m][1] * rs;
;                     if (kind <= 1) {
;                         float s = (v0[0] * v0[0] + v0[1] * v0[1]) + (v0[2] * v0[2] + v0[3] * v0[3]) + (v1[0] * v1[0] + v1[1] * v1[1]) + (v1[2] * v1[2] + v1[3] * v1[3]);
;                         s += __shfl_xor(s, 16); s += __shfl_xor(s, 32);
;                         const int head = (u.pn & 3) * 2 + bj;
;                         if (fq == 0) ssq[(size_t)((kind * 8 + head) * 4 + wc) * MT + row] = s;
;                     } else if (kind <= 3) {
;                         const int i0 = (c0 & 127) >> 1;
;                         const f32x4 csa = *(const f32x4*)(cs + (size_t)pos * 64 + i0), csb = *(const f32x4*)(cs + (size_t)pos * 64 + i0 + 2);
;                         const float sc = (kind == 3) ? KSCALE : 1.0f;
;                         f32x4 w0, w1;
;                         w0[0] = (v0[0] * csa[0] - v0[1] * csa[1]) * sc; w0[1] = (v0[1] * csa[0] + v0[0] * csa[1]) * sc;
;                         w0[2] = (v0[2] * csa[2] - v0[3] * csa[3]) * sc; w0[3] = (v0[3] * csa[2] + v0[2] * csa[3]) * sc;
;                         w1[0] = (v1[0] * csb[0] - v1[1] * csb[1]) * sc; w1[1] = (v1[1] * csb[0] + v1[0] * csb[1]) * sc;
;                         w1[2] = (v1[2] * csb[2] - v1[3] * csb[3]) * sc; w1[3] = (v1[3] * csb[2] + v1[2] * csb[3]) * sc;
;                         v0 = w0; v1 = w1;
;                     } else {
; #pragma unroll
;                         for (int j = 0; j < 4; ++j) { v0[j] = v0[j] * __builtin_amdgcn_rcpf(1.0f + __builtin_amdgcn_exp2f(-1.4426950408889634f * v0[j]));
;                                                       v1[j] = v1[j] * __builtin_amdgcn_rcpf(1.0f + __builtin_amdgcn_exp2f(-1.4426950408889634f * v1[j])); }
;                     }
;                     u32x4 w; w.x = cvt_pk_bf16(v0[0], v0[1]); w.y = cvt_pk_bf16(v0[2], v0[3]); w.z = cvt_pk_bf16(v1[0], v1[1]); w.w = cvt_pk_bf16(v1[2], v1[3]);
;                     *(u32x4*)(O + (size_t)row * TOKP + c0) = w;
.LBB0_296:
	v_mov_b64_e32 v[72:73], s[80:81]
	s_movk_i32 s0, 0x2900
	v_mad_i64_i32 v[72:73], s[0:1], v82, s0, v[72:73]
	v_cvt_pk_bf16_f32 v74, v84, v85
	v_cvt_pk_bf16_f32 v75, v86, v87
	v_lshl_add_u64 v[72:73], v[120:121], 1, v[72:73]
	v_mov_b32_e32 v81, v80
	v_cvt_pk_bf16_f32 v76, v88, v89
	v_cvt_pk_bf16_f32 v77, v90, v91
	v_and_b32_e32 v244, -16, v82
	v_mul_lo_u32 v244, v244, v233
	v_mov_b32_e32 v245, 0
	v_lshl_add_u64 v[246:247], v[244:245], 0, v[238:239]
	v_cndmask_b32_e64 v246, v72, v246, s[100:101]
	v_cndmask_b32_e64 v247, v73, v247, s[100:101]
	v_lshl_add_u64 v[248:249], v[246:247], 0, v[242:243]
	global_store_dwordx4 v[246:247], v[74:77], off
	v_pk_mul_f32 v[68:69], v[68:69], v[80:81]
	v_pk_mul_f32 v[64:65], v[64:65], v[80:81]
	v_mov_b32_e32 v74, v80
	v_mov_b32_e32 v75, v80
	v_pk_mul_f32 v[70:71], v[70:71], v[74:75]
	v_pk_mul_f32 v[66:67], v[66:67], v[74:75]
	s_and_b64 vcc, exec, s[40:41]
	s_mov_b64 s[0:1], -1
	s_cbranch_vccnz .LBB0_302
	s_and_b64 vcc, exec, s[38:39]
	s_cbranch_vccnz .LBB0_299
	v_mul_f32_e32 v75, 0xbfb8aa3b, v64
	v_mul_f32_e32 v76, 0xbfb8aa3b, v69
	v_exp_f32_e32 v75, v75
	v_exp_f32_e32 v76, v76
	v_mul_f32_e32 v77, 0xbfb8aa3b, v70
	v_mul_f32_e32 v79, 0xbfb8aa3b, v66
	v_add_f32_e32 v75, 1.0, v75
	v_rcp_f32_e32 v78, v75
	v_add_f32_e32 v75, 1.0, v76
	v_mul_f32_e32 v76, 0xbfb8aa3b, v65
	v_exp_f32_e32 v76, v76
	v_exp_f32_e32 v77, v77
	v_exp_f32_e32 v79, v79
	v_mul_f32_e32 v74, 0xbfb8aa3b, v68
	v_add_f32_e32 v82, 1.0, v76
	v_add_f32_e32 v76, 1.0, v77
	v_add_f32_e32 v77, 1.0, v79
	v_mul_f32_e32 v79, 0xbfb8aa3b, v71
	v_mul_f32_e32 v80, 0xbfb8aa3b, v67
	v_exp_f32_e32 v74, v74
	v_exp_f32_e32 v79, v79
	v_exp_f32_e32 v81, v80
	v_rcp_f32_e32 v80, v77
	v_add_f32_e32 v74, 1.0, v74
	v_add_f32_e32 v77, 1.0, v79
	v_add_f32_e32 v79, 1.0, v81
	v_rcp_f32_e32 v74, v74
	v_rcp_f32_e32 v75, v75
	v_rcp_f32_e32 v76, v76
	v_rcp_f32_e32 v77, v77
	v_rcp_f32_e32 v81, v79
	v_rcp_f32_e32 v79, v82
	v_pk_mul_f32 v[74:75], v[68:69], v[74:75]
	v_pk_mul_f32 v[76:77], v[70:71], v[76:77]
	v_pk_mul_f32 v[80:81], v[66:67], v[80:81]
	v_pk_mul_f32 v[78:79], v[64:65], v[78:79]
	s_mov_b64 s[0:1], 0

;     __device__ __forceinline__ void operator()(const f32x4 (&acc)[2][2][4][2], const Unit& u, int wr, int wc, int fr, int fq) const {
;     ...
;                 for (int bj = 0; bj < 2; ++bj) {
;                     const int c0 = u.pn * BM + bj * HALF + wc * 32 + 8 * fq;
;                     f32x4 v0 = acc[ai][bj][m][0] * rs, v1 = acc[ai][bj][m][1] * rs;
;                     if (kind <= 1) {
;                         float s = (v0[0] * v0[0] + v0[1] * v0[1]) + (v0[2] * v0[2] + v0[3] * v0[3]) + (v1[0] * v1[0] + v1[1] * v1[1]) + (v1[2] * v1[2] + v1[3] * v1[3]);
;                         s += __shfl_xor(s, 16); s += __shfl_xor(s, 32);
;                         const int head = (u.pn & 3) * 2 + bj;
;                         if (fq == 0) ssq[(size_t)((kind * 8 + head) * 4 + wc) * MT + row] = s;
;                     } else if (kind <= 3) {
;                         const int i0 = (c0 & 127) >> 1;
;                         const f32x4 csa = *(const f32x4*)(cs + (size_t)pos * 64 + i0), csb = *(const f32x4*)(cs + (size_t)pos * 64 + i0 + 2);
;                         const float sc = (kind == 3) ? KSCALE : 1.0f;
;                         f32x4 w0, w1;
;                         w0[0] = (v0[0] * csa[0] - v0[1] * csa[1]) * sc; w0[1] = (v0[1] * csa[0] + v0[0] * csa[1]) * sc;
;                         w0[2] = (v0[2] * csa[2] - v0[3] * csa[3]) * sc; w0[3] = (v0[3] * csa[2] + v0[2] * csa[3]) * sc;
;                         w1[0] = (v1[0] * csb[0] - v1[1] * csb[1]) * sc; w1[1] = (v1[1] * csb[0] + v1[0] * csb[1]) * sc;
;                         w1[2] = (v1[2] * csb[2] - v1[3] * csb[3]) * sc; w1[3] = (v1[3] * csb[2] + v1[2] * csb[3]) * sc;
;                         v0 = w0; v1 = w1;
;                     } else {
; #pragma unroll
;                         for (int j = 0; j < 4; ++j) { v0[j] = v0[j] * __builtin_amdgcn_rcpf(1.0f + __builtin_amdgcn_exp2f(-1.4426950408889634f * v0[j]));
;                                                       v1[j] = v1[j] * __builtin_amdgcn_rcpf(1.0f + __builtin_amdgcn_exp2f(-1.4426950408889634f * v1[j])); }
;                     }
;                     u32x4 w; w.x = cvt_pk_bf16(v0[0], v0[1]); w.y = cvt_pk_bf16(v0[2], v0[3]); w.z = cvt_pk_bf16(v1[0], v1[1]); w.w = cvt_pk_bf16(v1[2], v1[3]);
;                     *(u32x4*)(O + (size_t)row * TOKP + c0) = w;
.LBB0_316:
	v_mov_b64_e32 v[56:57], s[80:81]
	s_movk_i32 s0, 0x2900
	v_mad_i64_i32 v[56:57], s[0:1], v75, s0, v[56:57]
	v_cvt_pk_bf16_f32 v58, v66, v67
	v_cvt_pk_bf16_f32 v59, v68, v69
	v_lshl_add_u64 v[56:57], v[120:121], 1, v[56:57]
	v_mov_b32_e32 v65, v64
	v_cvt_pk_bf16_f32 v60, v70, v71
	v_cvt_pk_bf16_f32 v61, v72, v73
	v_and_b32_e32 v244, -16, v75
	v_mul_lo_u32 v244, v244, v233
	v_mov_b32_e32 v245, 0
	v_lshl_add_u64 v[246:247], v[244:245], 0, v[238:239]
	v_cndmask_b32_e64 v246, v56, v246, s[100:101]
	v_cndmask_b32_e64 v247, v57, v247, s[100:101]
	v_lshl_add_u64 v[248:249], v[246:247], 0, v[242:243]
	global_store_dwordx4 v[246:247], v[58:61], off
	v_pk_mul_f32 v[52:53], v[52:53], v[64:65]
	v_pk_mul_f32 v[48:49], v[48:49], v[64:65]
	v_mov_b32_e32 v58, v64
	v_mov_b32_e32 v59, v64
	v_pk_mul_f32 v[54:55], v[54:55], v[58:59]
	v_pk_mul_f32 v[50:51], v[50:51], v[58:59]
	s_and_b64 vcc, exec, s[40:41]
	s_mov_b64 s[0:1], -1
	s_cbranch_vccnz .LBB0_322
	s_and_b64 vcc, exec, s[38:39]
	s_cbranch_vccnz .LBB0_319
	v_mul_f32_e32 v59, 0xbfb8aa3b, v48
	v_mul_f32_e32 v60, 0xbfb8aa3b, v53
	v_exp_f32_e32 v59, v59
	v_exp_f32_e32 v60, v60
	v_mul_f32_e32 v61, 0xbfb8aa3b, v54
	v_mul_f32_e32 v63, 0xbfb8aa3b, v50
	v_add_f32_e32 v59, 1.0, v59
	v_rcp_f32_e32 v62, v59
	v_add_f32_e32 v59, 1.0, v60
	v_mul_f32_e32 v60, 0xbfb8aa3b, v49
	v_exp_f32_e32 v60, v60
	v_exp_f32_e32 v61, v61
	v_exp_f32_e32 v63, v63
	v_mul_f32_e32 v58, 0xbfb8aa3b, v52
	v_add_f32_e32 v66, 1.0, v60
	v_add_f32_e32 v60, 1.0, v61
	v_add_f32_e32 v61, 1.0, v63
	v_mul_f32_e32 v63, 0xbfb8aa3b, v55
	v_mul_f32_e32 v64, 0xbfb8aa3b, v51
	v_exp_f32_e32 v58, v58
	v_exp_f32_e32 v63, v63
	v_exp_f32_e32 v65, v64
	v_rcp_f32_e32 v64, v61
	v_add_f32_e32 v58, 1.0, v58
	v_add_f32_e32 v61, 1.0, v63
	v_add_f32_e32 v63, 1.0, v65
	v_rcp_f32_e32 v58, v58
	v_rcp_f32_e32 v59, v59
	v_rcp_f32_e32 v60, v60
	v_rcp_f32_e32 v61, v61
	v_rcp_f32_e32 v65, v63
	v_rcp_f32_e32 v63, v66
	v_pk_mul_f32 v[58:59], v[52:53], v[58:59]
	v_pk_mul_f32 v[60:61], v[54:55], v[60:61]
	v_pk_mul_f32 v[64:65], v[50:51], v[64:65]
	v_pk_mul_f32 v[62:63], v[48:49], v[62:63]
	s_mov_b64 s[0:1], 0

;     __device__ __forceinline__ void operator()(const f32x4 (&acc)[2][2][4][2], const Unit& u, int wr, int wc, int fr, int fq) const {
;     ...
;                 for (int bj = 0; bj < 2; ++bj) {
;                     const int c0 = u.pn * BM + bj * HALF + wc * 32 + 8 * fq;
;                     f32x4 v0 = acc[ai][bj][m][0] * rs, v1 = acc[ai][bj][m][1] * rs;
;                     if (kind <= 1) {
;                         float s = (v0[0] * v0[0] + v0[1] * v0[1]) + (v0[2] * v0[2] + v0[3] * v0[3]) + (v1[0] * v1[0] + v1[1] * v1[1]) + (v1[2] * v1[2] + v1[3] * v1[3]);
;                         s += __shfl_xor(s, 16); s += __shfl_xor(s, 32);
;                         const int head = (u.pn & 3) * 2 + bj;
;                         if (fq == 0) ssq[(size_t)((kind * 8 + head) * 4 + wc) * MT + row] = s;
;                     } else if (kind <= 3) {
;                         const int i0 = (c0 & 127) >> 1;
;                         const f32x4 csa = *(const f32x4*)(cs + (size_t)pos * 64 + i0), csb = *(const f32x4*)(cs + (size_t)pos * 64 + i0 + 2);
;                         const float sc = (kind == 3) ? KSCALE : 1.0f;
;                         f32x4 w0, w1;
;                         w0[0] = (v0[0] * csa[0] - v0[1] * csa[1]) * sc; w0[1] = (v0[1] * csa[0] + v0[0] * csa[1]) * sc;
;                         w0[2] = (v0[2] * csa[2] - v0[3] * csa[3]) * sc; w0[3] = (v0[3] * csa[2] + v0[2] * csa[3]) * sc;
;                         w1[0] = (v1[0] * csb[0] - v1[1] * csb[1]) * sc; w1[1] = (v1[1] * csb[0] + v1[0] * csb[1]) * sc;
;                         w1[2] = (v1[2] * csb[2] - v1[3] * csb[3]) * sc; w1[3] = (v1[3] * csb[2] + v1[2] * csb[3]) * sc;
;                         v0 = w0; v1 = w1;
;                     } else {
; #pragma unroll
;                         for (int j = 0; j < 4; ++j) { v0[j] = v0[j] * __builtin_amdgcn_rcpf(1.0f + __builtin_amdgcn_exp2f(-1.4426950408889634f * v0[j]));
;                                                       v1[j] = v1[j] * __builtin_amdgcn_rcpf(1.0f + __builtin_amdgcn_exp2f(-1.4426950408889634f * v1[j])); }
;                     }
;                     u32x4 w; w.x = cvt_pk_bf16(v0[0], v0[1]); w.y = cvt_pk_bf16(v0[2], v0[3]); w.z = cvt_pk_bf16(v1[0], v1[1]); w.w = cvt_pk_bf16(v1[2], v1[3]);
;                     *(u32x4*)(O + (size_t)row * TOKP + c0) = w;
.LBB0_336:
	v_mov_b64_e32 v[40:41], s[80:81]
	s_movk_i32 s0, 0x2900
	v_mad_i64_i32 v[40:41], s[0:1], v59, s0, v[40:41]
	v_cvt_pk_bf16_f32 v42, v50, v51
	v_cvt_pk_bf16_f32 v43, v52, v53
	v_lshl_add_u64 v[40:41], v[120:121], 1, v[40:41]
	v_mov_b32_e32 v49, v48
	v_cvt_pk_bf16_f32 v44, v54, v55
	v_cvt_pk_bf16_f32 v45, v56, v57
	v_and_b32_e32 v244, -16, v59
	v_mul_lo_u32 v244, v244, v233
	v_mov_b32_e32 v245, 0
	v_lshl_add_u64 v[246:247], v[244:245], 0, v[238:239]
	v_cndmask_b32_e64 v246, v40, v246, s[100:101]
	v_cndmask_b32_e64 v247, v41, v247, s[100:101]
	v_lshl_add_u64 v[248:249], v[246:247], 0, v[242:243]
	global_store_dwordx4 v[246:247], v[42:45], off
	v_pk_mul_f32 v[36:37], v[36:37], v[48:49]
	v_pk_mul_f32 v[32:33], v[32:33], v[48:49]
	v_mov_b32_e32 v42, v48
	v_mov_b32_e32 v43, v48
	v_pk_mul_f32 v[38:39], v[38:39], v[42:43]
	v_pk_mul_f32 v[34:35], v[34:35], v[42:43]
	s_and_b64 vcc, exec, s[40:41]
	s_mov_b64 s[0:1], -1
	s_cbranch_vccnz .LBB0_342
	s_and_b64 vcc, exec, s[38:39]
	s_cbranch_vccnz .LBB0_339
	v_mul_f32_e32 v43, 0xbfb8aa3b, v32
	v_mul_f32_e32 v44, 0xbfb8aa3b, v37
	v_exp_f32_e32 v43, v43
	v_exp_f32_e32 v44, v44
	v_mul_f32_e32 v45, 0xbfb8aa3b, v38
	v_mul_f32_e32 v47, 0xbfb8aa3b, v34
	v_add_f32_e32 v43, 1.0, v43
	v_rcp_f32_e32 v46, v43
	v_add_f32_e32 v43, 1.0, v44
	v_mul_f32_e32 v44, 0xbfb8aa3b, v33
	v_exp_f32_e32 v44, v44
	v_exp_f32_e32 v45, v45
	v_exp_f32_e32 v47, v47
	v_mul_f32_e32 v42, 0xbfb8aa3b, v36
	v_add_f32_e32 v50, 1.0, v44
	v_add_f32_e32 v44, 1.0, v45
	v_add_f32_e32 v45, 1.0, v47
	v_mul_f32_e32 v47, 0xbfb8aa3b, v39
	v_mul_f32_e32 v48, 0xbfb8aa3b, v35
	v_exp_f32_e32 v42, v42
	v_exp_f32_e32 v47, v47
	v_exp_f32_e32 v49, v48
	v_rcp_f32_e32 v48, v45
	v_add_f32_e32 v42, 1.0, v42
	v_add_f32_e32 v45, 1.0, v47
	v_add_f32_e32 v47, 1.0, v49
	v_rcp_f32_e32 v42, v42
	v_rcp_f32_e32 v43, v43
	v_rcp_f32_e32 v44, v44
	v_rcp_f32_e32 v45, v45
	v_rcp_f32_e32 v49, v47
	v_rcp_f32_e32 v47, v50
	v_pk_mul_f32 v[42:43], v[36:37], v[42:43]
	v_pk_mul_f32 v[44:45], v[38:39], v[44:45]
	v_pk_mul_f32 v[48:49], v[34:35], v[48:49]
	v_pk_mul_f32 v[46:47], v[32:33], v[46:47]
	s_mov_b64 s[0:1], 0

;     __device__ __forceinline__ void operator()(const f32x4 (&acc)[2][2][4][2], const Unit& u, int wr, int wc, int fr, int fq) const {
;     ...
;                 for (int bj = 0; bj < 2; ++bj) {
;                     const int c0 = u.pn * BM + bj * HALF + wc * 32 + 8 * fq;
;                     f32x4 v0 = acc[ai][bj][m][0] * rs, v1 = acc[ai][bj][m][1] * rs;
;                     if (kind <= 1) {
;                         float s = (v0[0] * v0[0] + v0[1] * v0[1]) + (v0[2] * v0[2] + v0[3] * v0[3]) + (v1[0] * v1[0] + v1[1] * v1[1]) + (v1[2] * v1[2] + v1[3] * v1[3]);
;                         s += __shfl_xor(s, 16); s += __shfl_xor(s, 32);
;                         const int head = (u.pn & 3) * 2 + bj;
;                         if (fq == 0) ssq[(size_t)((kind * 8 + head) * 4 + wc) * MT + row] = s;
;                     } else if (kind <= 3) {
;                         const int i0 = (c0 & 127) >> 1;
;                         const f32x4 csa = *(const f32x4*)(cs + (size_t)pos * 64 + i0), csb = *(const f32x4*)(cs + (size_t)pos * 64 + i0 + 2);
;                         const float sc = (kind == 3) ? KSCALE : 1.0f;
;                         f32x4 w0, w1;
;                         w0[0] = (v0[0] * csa[0] - v0[1] * csa[1]) * sc; w0[1] = (v0[1] * csa[0] + v0[0] * csa[1]) * sc;
;                         w0[2] = (v0[2] * csa[2] - v0[3] * csa[3]) * sc; w0[3] = (v0[3] * csa[2] + v0[2] * csa[3]) * sc;
;                         w1[0] = (v1[0] * csb[0] - v1[1] * csb[1]) * sc; w1[1] = (v1[1] * csb[0] + v1[0] * csb[1]) * sc;
;                         w1[2] = (v1[2] * csb[2] - v1[3] * csb[3]) * sc; w1[3] = (v1[3] * csb[2] + v1[2] * csb[3]) * sc;
;                         v0 = w0; v1 = w1;
;                     } else {
; #pragma unroll
;                         for (int j = 0; j < 4; ++j) { v0[j] = v0[j] * __builtin_amdgcn_rcpf(1.0f + __builtin_amdgcn_exp2f(-1.4426950408889634f * v0[j]));
;                                                       v1[j] = v1[j] * __builtin_amdgcn_rcpf(1.0f + __builtin_amdgcn_exp2f(-1.4426950408889634f * v1[j])); }
;                     }
;                     u32x4 w; w.x = cvt_pk_bf16(v0[0], v0[1]); w.y = cvt_pk_bf16(v0[2], v0[3]); w.z = cvt_pk_bf16(v1[0], v1[1]); w.w = cvt_pk_bf16(v1[2], v1[3]);
;                     *(u32x4*)(O + (size_t)row * TOKP + c0) = w;
.LBB0_356:
	v_mov_b64_e32 v[24:25], s[80:81]
	s_movk_i32 s0, 0x2900
	v_mad_i64_i32 v[24:25], s[0:1], v43, s0, v[24:25]
	v_cvt_pk_bf16_f32 v26, v34, v35
	v_cvt_pk_bf16_f32 v27, v36, v37
	v_lshl_add_u64 v[24:25], v[120:121], 1, v[24:25]
	v_mov_b32_e32 v33, v32
	v_cvt_pk_bf16_f32 v28, v38, v39
	v_cvt_pk_bf16_f32 v29, v40, v41
	v_and_b32_e32 v244, -16, v43
	v_mul_lo_u32 v244, v244, v233
	v_mov_b32_e32 v245, 0
	v_lshl_add_u64 v[246:247], v[244:245], 0, v[238:239]
	v_cndmask_b32_e64 v246, v24, v246, s[100:101]
	v_cndmask_b32_e64 v247, v25, v247, s[100:101]
	v_lshl_add_u64 v[248:249], v[246:247], 0, v[242:243]
	global_store_dwordx4 v[246:247], v[26:29], off
	v_pk_mul_f32 v[20:21], v[20:21], v[32:33]
	v_pk_mul_f32 v[16:17], v[16:17], v[32:33]
	v_mov_b32_e32 v26, v32
	v_mov_b32_e32 v27, v32
	v_pk_mul_f32 v[22:23], v[22:23], v[26:27]
	v_pk_mul_f32 v[18:19], v[18:19], v[26:27]
	s_and_b64 vcc, exec, s[40:41]
	s_mov_b64 s[0:1], -1
	s_cbranch_vccnz .LBB0_362
	s_and_b64 vcc, exec, s[38:39]
	s_cbranch_vccnz .LBB0_359
	v_mul_f32_e32 v27, 0xbfb8aa3b, v16
	v_mul_f32_e32 v28, 0xbfb8aa3b, v21
	v_exp_f32_e32 v27, v27
	v_exp_f32_e32 v28, v28
	v_mul_f32_e32 v29, 0xbfb8aa3b, v22
	v_mul_f32_e32 v31, 0xbfb8aa3b, v18
	v_add_f32_e32 v27, 1.0, v27
	v_rcp_f32_e32 v30, v27
	v_add_f32_e32 v27, 1.0, v28
	v_mul_f32_e32 v28, 0xbfb8aa3b, v17
	v_exp_f32_e32 v28, v28
	v_exp_f32_e32 v29, v29
	v_exp_f32_e32 v31, v31
	v_mul_f32_e32 v26, 0xbfb8aa3b, v20
	v_add_f32_e32 v34, 1.0, v28
	v_add_f32_e32 v28, 1.0, v29
	v_add_f32_e32 v29, 1.0, v31
	v_mul_f32_e32 v31, 0xbfb8aa3b, v23
	v_mul_f32_e32 v32, 0xbfb8aa3b, v19
	v_exp_f32_e32 v26, v26
	v_exp_f32_e32 v31, v31
	v_exp_f32_e32 v33, v32
	v_rcp_f32_e32 v32, v29
	v_add_f32_e32 v26, 1.0, v26
	v_add_f32_e32 v29, 1.0, v31
	v_add_f32_e32 v31, 1.0, v33
	v_rcp_f32_e32 v26, v26
	v_rcp_f32_e32 v27, v27
	v_rcp_f32_e32 v28, v28
	v_rcp_f32_e32 v29, v29
	v_rcp_f32_e32 v33, v31
	v_rcp_f32_e32 v31, v34
	v_pk_mul_f32 v[26:27], v[20:21], v[26:27]
	v_pk_mul_f32 v[28:29], v[22:23], v[28:29]
	v_pk_mul_f32 v[32:33], v[18:19], v[32:33]
	v_pk_mul_f32 v[30:31], v[16:17], v[30:31]
	s_mov_b64 s[0:1], 0

;     __device__ __forceinline__ void operator()(const f32x4 (&acc)[2][2][4][2], const Unit& u, int wr, int wc, int fr, int fq) const {
;     ...
;                 for (int bj = 0; bj < 2; ++bj) {
;                     const int c0 = u.pn * BM + bj * HALF + wc * 32 + 8 * fq;
;                     f32x4 v0 = acc[ai][bj][m][0] * rs, v1 = acc[ai][bj][m][1] * rs;
;                     if (kind <= 1) {
;                         float s = (v0[0] * v0[0] + v0[1] * v0[1]) + (v0[2] * v0[2] + v0[3] * v0[3]) + (v1[0] * v1[0] + v1[1] * v1[1]) + (v1[2] * v1[2] + v1[3] * v1[3]);
;                         s += __shfl_xor(s, 16); s += __shfl_xor(s, 32);
;                         const int head = (u.pn & 3) * 2 + bj;
;                         if (fq == 0) ssq[(size_t)((kind * 8 + head) * 4 + wc) * MT + row] = s;
;                     } else if (kind <= 3) {
;                         const int i0 = (c0 & 127) >> 1;
;                         const f32x4 csa = *(const f32x4*)(cs + (size_t)pos * 64 + i0), csb = *(const f32x4*)(cs + (size_t)pos * 64 + i0 + 2);
;                         const float sc = (kind == 3) ? KSCALE : 1.0f;
;                         f32x4 w0, w1;
;                         w0[0] = (v0[0] * csa[0] - v0[1] * csa[1]) * sc; w0[1] = (v0[1] * csa[0] + v0[0] * csa[1]) * sc;
;                         w0[2] = (v0[2] * csa[2] - v0[3] * csa[3]) * sc; w0[3] = (v0[3] * csa[2] + v0[2] * csa[3]) * sc;
;                         w1[0] = (v1[0] * csb[0] - v1[1] * csb[1]) * sc; w1[1] = (v1[1] * csb[0] + v1[0] * csb[1]) * sc;
;                         w1[2] = (v1[2] * csb[2] - v1[3] * csb[3]) * sc; w1[3] = (v1[3] * csb[2] + v1[2] * csb[3]) * sc;
;                         v0 = w0; v1 = w1;
;                     } else {
; #pragma unroll
;                         for (int j = 0; j < 4; ++j) { v0[j] = v0[j] * __builtin_amdgcn_rcpf(1.0f + __builtin_amdgcn_exp2f(-1.4426950408889634f * v0[j]));
;                                                       v1[j] = v1[j] * __builtin_amdgcn_rcpf(1.0f + __builtin_amdgcn_exp2f(-1.4426950408889634f * v1[j])); }
;                     }
;                     u32x4 w; w.x = cvt_pk_bf16(v0[0], v0[1]); w.y = cvt_pk_bf16(v0[2], v0[3]); w.z = cvt_pk_bf16(v1[0], v1[1]); w.w = cvt_pk_bf16(v1[2], v1[3]);
;                     *(u32x4*)(O + (size_t)row * TOKP + c0) = w;
.LBB0_376:
	v_mov_b64_e32 v[8:9], s[80:81]
	s_movk_i32 s0, 0x2900
	v_mad_i64_i32 v[8:9], s[0:1], v27, s0, v[8:9]
	v_cvt_pk_bf16_f32 v10, v18, v19
	v_cvt_pk_bf16_f32 v11, v20, v21
	v_lshl_add_u64 v[8:9], v[120:121], 1, v[8:9]
	v_mov_b32_e32 v17, v16
	v_cvt_pk_bf16_f32 v12, v22, v23
	v_cvt_pk_bf16_f32 v13, v24, v25
	v_and_b32_e32 v244, -16, v27
	v_mul_lo_u32 v244, v244, v233
	v_mov_b32_e32 v245, 0
	v_lshl_add_u64 v[246:247], v[244:245], 0, v[238:239]
	v_cndmask_b32_e64 v246, v8, v246, s[100:101]
	v_cndmask_b32_e64 v247, v9, v247, s[100:101]
	v_lshl_add_u64 v[248:249], v[246:247], 0, v[242:243]
	global_store_dwordx4 v[246:247], v[10:13], off
	s_and_b64 vcc, exec, s[40:41]
	v_readlane_b32 s40, v250, 32
	v_mov_b32_e32 v10, v16
	v_mov_b32_e32 v11, v16
	v_pk_mul_f32 v[6:7], v[6:7], v[10:11]
	v_pk_mul_f32 v[4:5], v[4:5], v[16:17]
	v_pk_mul_f32 v[2:3], v[2:3], v[10:11]
	v_pk_mul_f32 v[0:1], v[0:1], v[16:17]
	s_mov_b64 s[0:1], -1
	v_readlane_b32 s41, v250, 33
	s_cbranch_vccnz .LBB0_382
	s_and_b64 vcc, exec, s[38:39]
	s_cbranch_vccnz .LBB0_379
	v_mul_f32_e32 v11, 0xbfb8aa3b, v0
	v_mul_f32_e32 v12, 0xbfb8aa3b, v5
	v_exp_f32_e32 v11, v11
	v_exp_f32_e32 v12, v12
	v_mul_f32_e32 v13, 0xbfb8aa3b, v6
	v_mul_f32_e32 v15, 0xbfb8aa3b, v2
	v_add_f32_e32 v11, 1.0, v11
	v_rcp_f32_e32 v14, v11
	v_add_f32_e32 v11, 1.0, v12
	v_mul_f32_e32 v12, 0xbfb8aa3b, v1
	v_exp_f32_e32 v12, v12
	v_exp_f32_e32 v13, v13
	v_exp_f32_e32 v15, v15
	v_mul_f32_e32 v10, 0xbfb8aa3b, v4
	v_add_f32_e32 v18, 1.0, v12
	v_add_f32_e32 v12, 1.0, v13
	v_add_f32_e32 v13, 1.0, v15
	v_mul_f32_e32 v15, 0xbfb8aa3b, v7
	v_mul_f32_e32 v16, 0xbfb8aa3b, v3
	v_exp_f32_e32 v10, v10
	v_exp_f32_e32 v15, v15
	v_exp_f32_e32 v17, v16
	v_rcp_f32_e32 v16, v13
	v_add_f32_e32 v10, 1.0, v10
	v_add_f32_e32 v13, 1.0, v15
	v_add_f32_e32 v15, 1.0, v17
	v_rcp_f32_e32 v10, v10
	v_rcp_f32_e32 v11, v11
	v_rcp_f32_e32 v12, v12
	v_rcp_f32_e32 v13, v13
	v_rcp_f32_e32 v17, v15
	v_rcp_f32_e32 v15, v18
	v_pk_mul_f32 v[10:11], v[4:5], v[10:11]
	v_pk_mul_f32 v[12:13], v[6:7], v[12:13]
	v_pk_mul_f32 v[16:17], v[2:3], v[16:17]
	v_pk_mul_f32 v[14:15], v[0:1], v[14:15]
	s_mov_b64 s[0:1], 0

; #define GAS __attribute__((address_space(1)))
; __device__ __forceinline__ void attn_wg_task(const Frame& F, int l, int task) {
;     ...
;     bf16x8 Qf[2][4];
; #pragma unroll
;     for (int qb = 0; qb < 2; ++qb) {
;         const int tq = tq0 + qb * 16;
;         float ssq = 0.f;
; #pragma unroll
;         for (int w = 0; w < 4; ++w) ssq += *(const GAS float*)(SSQ + (size_t)((0 * 8 + h) * 4 + w) * T + tq);
;         const float rs = frsq(ssq * (1.f / HD) + EPS) * (pg8::KSCALE * LOG2E);
; #pragma unroll
;         for (int ks = 0; ks < 4; ++ks) {
;             const float* gp = F.qa_g + l * HD + ks * 32 + rq * 8; const float* kp = F.ka_g + l * HD + ks * 32 + rq * 8;
;             const f32x4 a0 = ld_f4(gp), a1 = ld_f4(gp + 4), b0 = ld_f4(kp), b1 = ld_f4(kp + 4);
;             const u32x4 raw = ld_u4(TOK + (size_t)tq * TOKP + TK_QA + h * HD + ks * 32 + rq * 8);
;             u32x4 o;
;             o.x = pk2(bf_lo(raw.x) * rs * (a0[0] * b0[0]), bf_hi(raw.x) * rs * (a0[1] * b0[1])); o.y = pk2(bf_lo(raw.y) * rs * (a0[2] * b0[2]), bf_hi(raw.y) * rs * (a0[3] * b0[3]));
;             o.z = pk2(bf_lo(raw.z) * rs * (a1[0] * b1[0]), bf_hi(raw.z) * rs * (a1[1] * b1[1])); o.w = pk2(bf_lo(raw.w) * rs * (a1[2] * b1[2]), bf_hi(raw.w) * rs * (a1[3] * b1[3]));
;             Qf[qb][ks] = __builtin_bit_cast(bf16x8, o);
;         }
;     ...
;     const int p0 = tid, p1 = tid + 512;
;     const int kr0 = p0 >> 4, kr1 = p1 >> 4;
;     const int kl0 = (kr0 & 32) + ((kr0 >> 2) & 1) * 16 + ((kr0 >> 3) & 3) * 4 + (kr0 & 3), kl1 = (kr1 & 32) + ((kr1 >> 2) & 1) * 16 + ((kr1 >> 3) & 3) * 4 + (kr1 & 3);
;     const bf16* gk0 = TOK + (size_t)(b * S + kr0) * TOKP + TK_KA + h * HD + (p0 & 15) * 8; const bf16* gk1 = TOK + (size_t)(b * S + kr1) * TOKP + TK_KA + h * HD + (p1 & 15) * 8;
;     const bf16* gv0 = SWP + (size_t)(SW_VA + h * HD + (p0 >> 3)) * SWPP + b * S + (p0 & 7) * 8; const bf16* gv1 = SWP + (size_t)(SW_VA + h * HD + (p1 >> 3)) * SWPP + b * S + (p1 & 7) * 8;
;     const int lk0 = A_KBUF + kl0 * A_KP + (p0 & 15) * 16, lk1 = A_KBUF + kl1 * A_KP + (p1 & 15) * 16;
;     const int lv0 = A_VBUF + (p0 >> 3) * A_VP + (p0 & 7) * 16, lv1 = A_VBUF + (p1 >> 3) * A_VP + (p1 & 7) * 16;
;     const float* gss = SSQ + (size_t)((8 + h) * 4) * T + b * S + (tid & 63);
;     u32x4 r0, r1, r2, r3; float rkv = 0.f;
;     const int kc0 = 4 * cq - 8, j0 = kc0 < 0 ? -kc0 : 0;
.LBB0_521:
	s_lshl_b32 s1, s19, 2
	s_and_b32 s21, s1, 28
	s_lshl_b32 s20, s19, 5
	s_add_i32 s1, s21, s25
	s_waitcnt vmcnt(0)
	v_mov_b32_e32 v123, v212
	s_bfe_u32 s4, s19, 0x30003
	s_and_b32 s0, s20, 0xfffff800
	s_lshl_b32 s1, s1, 6
	s_add_i32 s1, s1, s0
	v_and_b32_e32 v122, 15, v123
	s_lshl_b32 s17, s4, 7
	s_lshl_b32 s96, s4, 8
	v_or_b32_e32 v207, s66, v122
	s_add_u32 s2, s80, s96
	v_or_b32_e32 v152, s1, v207
	s_addc_u32 s3, s81, 0
	v_and_b32_e32 v184, 48, v123
	s_waitcnt lgkmcnt(0)
	v_lshl_add_u64 v[0:1], s[2:3], 0, v[184:185]
	v_ashrrev_i32_e32 v153, 31, v152
	s_lshl_b32 s2, s4, 18
	v_bfe_u32 v204, v123, 4, 2
	v_lshl_add_u64 v[2:3], v[152:153], 2, s[88:89]
	s_mov_b32 s3, s97
	s_or_b32 s8, s2, 0x10000
	s_mov_b32 s9, s97
	s_or_b32 s14, s2, 0x20000
	s_mov_b32 s15, s97
	s_or_b32 s22, s2, 0x30000
	s_mov_b32 s23, s97
	v_lshlrev_b32_e32 v206, 5, v204
	v_lshl_add_u64 v[4:5], v[2:3], 0, s[2:3]
	v_lshl_add_u64 v[6:7], v[2:3], 0, s[8:9]
	v_lshl_add_u64 v[8:9], v[2:3], 0, s[14:15]
	v_lshl_add_u64 v[2:3], v[2:3], 0, s[22:23]
	s_movk_i32 s1, 0x2900
	global_load_dword v64, v[4:5], off
	global_load_dword v65, v[6:7], off
	global_load_dword v70, v[8:9], off
	global_load_dword v71, v[2:3], off
	v_mad_i64_i32 v[2:3], s[12:13], v152, s1, v[0:1]
	v_and_b32_e32 v240, -16, v152
	v_add_u32_e32 v240, s4, v240
	v_mul_u32_u24_e32 v240, 0x2900, v240
	v_and_b32_e32 v241, 15, v152
	v_lshl_add_u32 v240, v241, 4, v240
	v_lshl_add_u32 v240, v204, 8, v240
	v_add_u32_e32 v240, 0x12001000, v240
	v_mov_b32_e32 v241, 0
	v_lshl_add_u64 v[2:3], s[62:63], 0, v[240:241]
	v_mov_b32_e32 v240, 0x29000
	v_lshl_add_u64 v[242:243], v[2:3], 0, v[240:241]
	global_load_dwordx4 v[84:87], v206, s[38:39] offset:16
	global_load_dwordx4 v[92:95], v206, s[38:39]
	global_load_dwordx4 v[88:91], v206, s[40:41] offset:16
	global_load_dwordx4 v[96:99], v206, s[40:41]
	global_load_dwordx4 v[56:59], v206, s[38:39] offset:144
	global_load_dwordx4 v[72:75], v206, s[38:39] offset:128
	global_load_dwordx4 v[60:63], v206, s[40:41] offset:144
	global_load_dwordx4 v[76:79], v206, s[40:41] offset:128
	global_load_dwordx4 v[80:83], v[2:3], off
	global_load_dwordx4 v[52:55], v[2:3], off offset:1024
	global_load_dwordx4 v[32:35], v206, s[38:39] offset:272
	global_load_dwordx4 v[40:43], v206, s[38:39] offset:256
	global_load_dwordx4 v[36:39], v206, s[40:41] offset:272
	global_load_dwordx4 v[44:47], v206, s[40:41] offset:256
	global_load_dwordx4 v[8:11], v206, s[38:39] offset:400
	global_load_dwordx4 v[16:19], v206, s[38:39] offset:384
	s_waitcnt lgkmcnt(0)
	global_load_dwordx4 v[12:15], v206, s[40:41] offset:400
	global_load_dwordx4 v[20:23], v206, s[40:41] offset:384
	global_load_dwordx4 v[28:31], v[2:3], off offset:2048
	global_load_dwordx4 v[4:7], v[2:3], off offset:3072
	v_add_u32_e32 v110, 0x200, v123
	s_waitcnt vmcnt(32)
	v_ashrrev_i32_e32 v132, 4, v123
	v_ashrrev_i32_e32 v131, 4, v110
	v_add_u32_e32 v128, s0, v132
	v_mov_b64_e32 v[100:101], s[80:81]
	v_add_u32_e32 v129, s0, v131
	v_or_b32_e32 v148, 16, v152
	s_add_u32 s12, s88, s2
	v_mad_i64_i32 v[102:103], s[2:3], v128, s1, v[100:101]
	v_mad_i64_i32 v[100:101], s[2:3], v129, s1, v[100:101]
	v_ashrrev_i32_e32 v149, 31, v148
	v_lshl_add_u64 v[102:103], v[102:103], 0, s[96:97]
	v_lshlrev_b32_e32 v116, 4, v122
	v_mov_b32_e32 v117, v185
	v_lshl_add_u64 v[100:101], v[100:101], 0, s[96:97]
	v_ashrrev_i32_e32 v133, 3, v123
	v_lshlrev_b64 v[2:3], 2, v[148:149]
	v_lshl_add_u64 v[102:103], v[102:103], 0, v[116:117]
	v_lshl_add_u64 v[100:101], v[100:101], 0, v[116:117]
	v_add_u32_e32 v117, s17, v133
	v_mov_b64_e32 v[104:105], s[64:65]
	s_mov_b32 s5, 0x8100
	v_ashrrev_i32_e32 v134, 3, v110
	v_lshl_add_u64 v[24:25], s[88:89], 0, v[2:3]
	s_addc_u32 s13, s89, 0
	v_mad_i64_i32 v[0:1], s[2:3], v148, s1, v[0:1]
	v_mov_b32_e32 v0, v242
	v_mov_b32_e32 v1, v243
	v_mad_i64_i32 v[106:107], s[2:3], v117, s5, v[104:105]
	s_ashr_i32 s1, s0, 31
	v_add_u32_e32 v130, s17, v134
	v_lshl_add_u64 v[26:27], v[24:25], 0, s[8:9]
	s_lshl_b64 s[2:3], s[0:1], 1
	v_and_b32_e32 v108, 7, v123
	v_mad_i64_i32 v[104:105], s[8:9], v130, s5, v[104:105]
	v_lshlrev_b32_e32 v118, 4, v108
	v_mov_b32_e32 v119, v185
	v_lshl_add_u64 v[104:105], v[104:105], 0, s[2:3]
	v_lshl_add_u64 v[110:111], v[104:105], 0, v[118:119]
	v_sub_u32_e64 v104, 8, s21 clamp
	v_lshl_add_u64 v[48:49], v[24:25], 0, s[14:15]
	v_readfirstlane_b32 s18, v104
	s_add_i32 s5, s21, s18
	s_lshl_b32 s5, s5, 6
	s_add_i32 s14, s5, 0xfffffe00
	v_lshl_add_u64 v[2:3], s[12:13], 0, v[2:3]
	v_lshl_add_u64 v[24:25], v[24:25], 0, s[22:23]
	v_lshl_add_u64 v[106:107], v[106:107], 0, s[2:3]
	s_ashr_i32 s15, s14, 31
	v_mad_i64_i32 v[102:103], s[8:9], s14, v223, v[102:103]
	v_mad_i64_i32 v[100:101], s[8:9], s14, v223, v[100:101]
	global_load_dword v124, v[2:3], off
	global_load_dword v125, v[26:27], off
	global_load_dword v126, v[48:49], off
	global_load_dword v127, v[24:25], off
	global_load_dwordx4 v[66:69], v[0:1], off
	s_nop 0
	global_load_dwordx4 v[48:51], v[0:1], off offset:1024
	global_load_dwordx4 v[24:27], v[0:1], off offset:2048
	s_nop 0
	global_load_dwordx4 v[0:3], v[0:1], off offset:3072
	v_lshl_add_u64 v[108:109], v[106:107], 0, v[118:119]
	s_lshl_b64 s[8:9], s[14:15], 1
	v_lshl_add_u64 v[108:109], v[108:109], 0, s[8:9]
	v_lshl_add_u64 v[110:111], v[110:111], 0, s[8:9]
	s_barrier
	global_load_dwordx4 v[104:107], v[102:103], off offset:2048
	s_nop 0
	global_load_dwordx4 v[100:103], v[100:101], off offset:2048
	s_nop 0
	global_load_dwordx4 v[112:115], v[108:109], off
	s_nop 0
	global_load_dwordx4 v[108:111], v[110:111], off
	v_and_b32_e32 v119, 63, v123
	v_mov_b32_e32 v228, 0
	v_cmp_gt_i32_e64 s[34:35], 64, v123
	v_lshlrev_b32_e32 v120, 2, v119
	s_and_saveexec_b64 s[8:9], s[34:35]
	s_cbranch_execz .LBB0_523
	s_lshl_b64 s[22:23], s[0:1], 2
	s_add_u32 s12, s12, s22
	s_addc_u32 s13, s13, s23
	v_mov_b32_e32 v121, v185
	v_lshl_add_u64 v[136:137], s[12:13], 0, v[120:121]
	v_lshl_add_u64 v[136:137], s[14:15], 2, v[136:137]
	v_add_co_u32_e32 v138, vcc, 0x200000, v136
	s_nop 1
	v_addc_co_u32_e32 v139, vcc, 0, v137, vcc
	global_load_dword v119, v[138:139], off
	v_add_co_u32_e32 v138, vcc, 0x210000, v136
	s_nop 1
	v_addc_co_u32_e32 v139, vcc, 0, v137, vcc
	global_load_dword v121, v[138:139], off
	v_add_co_u32_e32 v138, vcc, 0x220000, v136
	s_nop 1
	v_addc_co_u32_e32 v139, vcc, 0, v137, vcc
	global_load_dword v240, v[138:139], off
	v_add_co_u32_e32 v136, vcc, 0x230000, v136
	s_nop 1
	v_addc_co_u32_e32 v137, vcc, 0, v137, vcc
	global_load_dword v241, v[136:137], off
	s_waitcnt vmcnt(0)
	v_add_f32_e32 v119, 0, v119
	v_add_f32_e32 v119, v119, v121
	s_nop 0
	v_add_f32_e32 v119, v119, v240
	s_nop 0
	v_add_f32_e32 v119, v119, v241
	v_fmamk_f32 v119, v119, 0x3c000000, v214
	v_rsq_f32_e32 v228, v119

; #define GAS __attribute__((address_space(1)))
; __device__ __forceinline__ void attn_wg_task(const Frame& F, int l, int task) {
;     ...
;     bf16x8 Qf[2][4];
; #pragma unroll
;     for (int qb = 0; qb < 2; ++qb) {
;         const int tq = tq0 + qb * 16;
;         float ssq = 0.f;
; #pragma unroll
;         for (int w = 0; w < 4; ++w) ssq += *(const GAS float*)(SSQ + (size_t)((0 * 8 + h) * 4 + w) * T + tq);
;         const float rs = frsq(ssq * (1.f / HD) + EPS) * (pg8::KSCALE * LOG2E);
; #pragma unroll
;         for (int ks = 0; ks < 4; ++ks) {
;             const float* gp = F.qa_g + l * HD + ks * 32 + rq * 8; const float* kp = F.ka_g + l * HD + ks * 32 + rq * 8;
;             const f32x4 a0 = ld_f4(gp), a1 = ld_f4(gp + 4), b0 = ld_f4(kp), b1 = ld_f4(kp + 4);
;             const u32x4 raw = ld_u4(TOK + (size_t)tq * TOKP + TK_QA + h * HD + ks * 32 + rq * 8);
;             u32x4 o;
;             o.x = pk2(bf_lo(raw.x) * rs * (a0[0] * b0[0]), bf_hi(raw.x) * rs * (a0[1] * b0[1])); o.y = pk2(bf_lo(raw.y) * rs * (a0[2] * b0[2]), bf_hi(raw.y) * rs * (a0[3] * b0[3]));
;             o.z = pk2(bf_lo(raw.z) * rs * (a1[0] * b1[0]), bf_hi(raw.z) * rs * (a1[1] * b1[1])); o.w = pk2(bf_lo(raw.w) * rs * (a1[2] * b1[2]), bf_hi(raw.w) * rs * (a1[3] * b1[3]));
;             Qf[qb][ks] = __builtin_bit_cast(bf16x8, o);
;         }
;     ...
;     const int p0 = tid, p1 = tid + 512;
;     const int kr0 = p0 >> 4, kr1 = p1 >> 4;
;     const int kl0 = (kr0 & 32) + ((kr0 >> 2) & 1) * 16 + ((kr0 >> 3) & 3) * 4 + (kr0 & 3), kl1 = (kr1 & 32) + ((kr1 >> 2) & 1) * 16 + ((kr1 >> 3) & 3) * 4 + (kr1 & 3);
;     const bf16* gk0 = TOK + (size_t)(b * S + kr0) * TOKP + TK_KA + h * HD + (p0 & 15) * 8; const bf16* gk1 = TOK + (size_t)(b * S + kr1) * TOKP + TK_KA + h * HD + (p1 & 15) * 8;
;     const bf16* gv0 = SWP + (size_t)(SW_VA + h * HD + (p0 >> 3)) * SWPP + b * S + (p0 & 7) * 8; const bf16* gv1 = SWP + (size_t)(SW_VA + h * HD + (p1 >> 3)) * SWPP + b * S + (p1 & 7) * 8;
;     const int lk0 = A_KBUF + kl0 * A_KP + (p0 & 15) * 16, lk1 = A_KBUF + kl1 * A_KP + (p1 & 15) * 16;
;     const int lv0 = A_VBUF + (p0 >> 3) * A_VP + (p0 & 7) * 16, lv1 = A_VBUF + (p1 >> 3) * A_VP + (p1 & 7) * 16;
;     const float* gss = SSQ + (size_t)((8 + h) * 4) * T + b * S + (tid & 63);
;     u32x4 r0, r1, r2, r3; float rkv = 0.f;
;     const int kc0 = 4 * cq - 8, j0 = kc0 < 0 ? -kc0 : 0;
.LBB0_550:
	s_lshl_b32 s1, s18, 2
	s_and_b32 s22, s1, 28
	s_lshl_b32 s0, s18, 5
	s_add_i32 s1, s22, s25
	s_waitcnt vmcnt(0)
	v_mov_b32_e32 v116, v212
	s_bfe_u32 s20, s18, 0x30003
	s_and_b32 s0, s0, 0xfffff800
	s_lshl_b32 s1, s1, 6
	s_add_i32 s1, s1, s0
	v_and_b32_e32 v117, 15, v116
	s_lshl_b32 s19, s20, 7
	s_lshl_b32 s96, s20, 8
	v_or_b32_e32 v207, s66, v117
	s_add_u32 s2, s80, s96
	v_or_b32_e32 v152, s1, v207
	s_addc_u32 s3, s81, 0
	v_and_b32_e32 v184, 48, v116
	s_waitcnt lgkmcnt(0)
	v_lshl_add_u64 v[0:1], s[2:3], 0, v[184:185]
	v_ashrrev_i32_e32 v153, 31, v152
	s_lshl_b32 s2, s20, 18
	v_bfe_u32 v204, v116, 4, 2
	v_lshl_add_u64 v[2:3], v[152:153], 2, s[88:89]
	s_mov_b32 s3, s97
	s_or_b32 s4, s2, 0x10000
	s_mov_b32 s5, s97
	s_or_b32 s12, s2, 0x20000
	s_mov_b32 s13, s97
	s_or_b32 s14, s2, 0x30000
	s_mov_b32 s15, s97
	v_lshlrev_b32_e32 v206, 5, v204
	v_lshl_add_u64 v[4:5], v[2:3], 0, s[2:3]
	v_lshl_add_u64 v[6:7], v[2:3], 0, s[4:5]
	v_lshl_add_u64 v[8:9], v[2:3], 0, s[12:13]
	v_lshl_add_u64 v[2:3], v[2:3], 0, s[14:15]
	s_movk_i32 s1, 0x2900
	global_load_dword v123, v[4:5], off
	global_load_dword v124, v[6:7], off
	global_load_dword v125, v[8:9], off
	global_load_dword v126, v[2:3], off
	v_mad_i64_i32 v[2:3], s[8:9], v152, s1, v[0:1]
	v_and_b32_e32 v240, -16, v152
	v_add_u32_e32 v240, s20, v240
	v_mul_u32_u24_e32 v240, 0x2900, v240
	v_and_b32_e32 v241, 15, v152
	v_lshl_add_u32 v240, v241, 4, v240
	v_lshl_add_u32 v240, v204, 8, v240
	v_add_u32_e32 v240, 0x12001000, v240
	v_mov_b32_e32 v241, 0
	v_lshl_add_u64 v[2:3], s[62:63], 0, v[240:241]
	v_mov_b32_e32 v240, 0x29000
	v_lshl_add_u64 v[242:243], v[2:3], 0, v[240:241]
	global_load_dwordx4 v[84:87], v206, s[38:39] offset:16
	global_load_dwordx4 v[92:95], v206, s[38:39]
	global_load_dwordx4 v[88:91], v206, s[40:41] offset:16
	global_load_dwordx4 v[96:99], v206, s[40:41]
	global_load_dwordx4 v[56:59], v206, s[38:39] offset:144
	global_load_dwordx4 v[72:75], v206, s[38:39] offset:128
	global_load_dwordx4 v[60:63], v206, s[40:41] offset:144
	global_load_dwordx4 v[76:79], v206, s[40:41] offset:128
	global_load_dwordx4 v[80:83], v[2:3], off
	global_load_dwordx4 v[52:55], v[2:3], off offset:1024
	global_load_dwordx4 v[32:35], v206, s[38:39] offset:272
	global_load_dwordx4 v[40:43], v206, s[38:39] offset:256
	global_load_dwordx4 v[36:39], v206, s[40:41] offset:272
	global_load_dwordx4 v[44:47], v206, s[40:41] offset:256
	global_load_dwordx4 v[8:11], v206, s[38:39] offset:400
	global_load_dwordx4 v[16:19], v206, s[38:39] offset:384
	s_waitcnt lgkmcnt(0)
	global_load_dwordx4 v[12:15], v206, s[40:41] offset:400
	global_load_dwordx4 v[20:23], v206, s[40:41] offset:384
	global_load_dwordx4 v[28:31], v[2:3], off offset:2048
	global_load_dwordx4 v[4:7], v[2:3], off offset:3072
	v_add_u32_e32 v110, 0x200, v116
	v_or_b32_e32 v148, 16, v152
	v_ashrrev_i32_e32 v118, 4, v116
	v_ashrrev_i32_e32 v119, 4, v110
	v_ashrrev_i32_e32 v149, 31, v148
	s_waitcnt vmcnt(35)
	v_add_u32_e32 v64, s0, v118
	s_waitcnt vmcnt(34)
	v_mov_b64_e32 v[70:71], s[80:81]
	v_add_u32_e32 v102, s0, v119
	v_lshlrev_b64 v[2:3], 2, v[148:149]
	s_add_u32 s8, s88, s2
	v_mad_i64_i32 v[64:65], s[2:3], v64, s1, v[70:71]
	v_mad_i64_i32 v[70:71], s[2:3], v102, s1, v[70:71]
	v_lshl_add_u64 v[24:25], s[88:89], 0, v[2:3]
	v_lshl_add_u64 v[100:101], v[64:65], 0, s[96:97]
	v_lshlrev_b32_e32 v64, 4, v117
	v_mov_b32_e32 v65, v185
	v_lshl_add_u64 v[70:71], v[70:71], 0, s[96:97]
	v_ashrrev_i32_e32 v121, 3, v116
	v_lshl_add_u64 v[26:27], v[24:25], 0, s[4:5]
	v_lshl_add_u64 v[100:101], v[100:101], 0, v[64:65]
	v_lshl_add_u64 v[102:103], v[70:71], 0, v[64:65]
	v_add_u32_e32 v65, s19, v121
	v_mov_b64_e32 v[104:105], s[64:65]
	s_mov_b32 s4, 0x8100
	s_addc_u32 s9, s89, 0
	v_mad_i64_i32 v[0:1], s[2:3], v148, s1, v[0:1]
	v_mov_b32_e32 v0, v242
	v_mov_b32_e32 v1, v243
	v_mad_i64_i32 v[70:71], s[2:3], v65, s4, v[104:105]
	s_ashr_i32 s1, s0, 31
	s_lshl_b64 s[2:3], s[0:1], 1
	v_and_b32_e32 v65, 7, v116
	v_ashrrev_i32_e32 v120, 3, v110
	v_lshl_add_u64 v[106:107], v[70:71], 0, s[2:3]
	v_lshlrev_b32_e32 v70, 4, v65
	v_add_u32_e32 v65, s19, v120
	v_mad_i64_i32 v[104:105], s[4:5], v65, s4, v[104:105]
	v_sub_u32_e64 v65, 8, s22 clamp
	v_lshl_add_u64 v[104:105], v[104:105], 0, s[2:3]
	v_readfirstlane_b32 s21, v65
	s_add_i32 s22, s22, s21
	s_lshl_b32 s2, s22, 6
	s_waitcnt vmcnt(33)
	v_lshl_add_u64 v[48:49], v[24:25], 0, s[12:13]
	s_add_i32 s12, s2, 0xfffffe00
	v_lshl_add_u64 v[2:3], s[8:9], 0, v[2:3]
	v_lshl_add_u64 v[24:25], v[24:25], 0, s[14:15]
	v_mov_b32_e32 v71, v185
	s_ashr_i32 s13, s12, 31
	v_mad_i64_i32 v[100:101], s[2:3], s12, v223, v[100:101]
	v_mad_i64_i32 v[102:103], s[2:3], s12, v223, v[102:103]
	global_load_dword v127, v[2:3], off
	global_load_dword v128, v[26:27], off
	global_load_dword v129, v[48:49], off
	global_load_dword v130, v[24:25], off
	global_load_dwordx4 v[66:69], v[0:1], off
	s_nop 0
	global_load_dwordx4 v[48:51], v[0:1], off offset:1024
	global_load_dwordx4 v[24:27], v[0:1], off offset:2048
	s_nop 0
	global_load_dwordx4 v[0:3], v[0:1], off offset:3072
	v_lshl_add_u64 v[108:109], v[106:107], 0, v[70:71]
	v_lshl_add_u64 v[110:111], v[104:105], 0, v[70:71]
	s_lshl_b64 s[2:3], s[12:13], 1
	v_lshl_add_u64 v[108:109], v[108:109], 0, s[2:3]
	v_lshl_add_u64 v[110:111], v[110:111], 0, s[2:3]
	s_barrier
	global_load_dwordx4 v[104:107], v[100:101], off offset:2048
	s_nop 0
	global_load_dwordx4 v[100:103], v[102:103], off offset:2048
	s_nop 0
	global_load_dwordx4 v[112:115], v[108:109], off
	s_nop 0
	global_load_dwordx4 v[108:111], v[110:111], off
	v_and_b32_e32 v122, 63, v116
	v_mov_b32_e32 v228, 0
	v_cmp_gt_i32_e64 s[34:35], 64, v116
	s_and_saveexec_b64 s[2:3], s[34:35]
	s_cbranch_execz .LBB0_552
	s_lshl_b64 s[0:1], s[0:1], 2
	s_add_u32 s0, s8, s0
	s_addc_u32 s1, s9, s1
	s_waitcnt vmcnt(44)
	v_lshlrev_b32_e32 v132, 2, v122
	v_mov_b32_e32 v133, v185
	v_lshl_add_u64 v[132:133], s[0:1], 0, v[132:133]
	v_lshl_add_u64 v[132:133], s[12:13], 2, v[132:133]
	v_add_co_u32_e32 v134, vcc, 0x200000, v132
	s_nop 1
	v_addc_co_u32_e32 v135, vcc, 0, v133, vcc
	global_load_dword v65, v[134:135], off
	v_add_co_u32_e32 v134, vcc, 0x210000, v132
	s_nop 1
	v_addc_co_u32_e32 v135, vcc, 0, v133, vcc
	global_load_dword v71, v[134:135], off
	v_add_co_u32_e32 v134, vcc, 0x220000, v132
	s_nop 1
	v_addc_co_u32_e32 v135, vcc, 0, v133, vcc
	global_load_dword v240, v[134:135], off
	v_add_co_u32_e32 v132, vcc, 0x230000, v132
	s_nop 1
	v_addc_co_u32_e32 v133, vcc, 0, v133, vcc
	global_load_dword v241, v[132:133], off
	s_waitcnt vmcnt(0)
	v_add_f32_e32 v65, 0, v65
	v_add_f32_e32 v65, v65, v71
	s_nop 0
	v_add_f32_e32 v65, v65, v240
	s_nop 0
	v_add_f32_e32 v65, v65, v241
	v_fmamk_f32 v65, v65, 0x3c000000, v214
	v_rsq_f32_e32 v228, v65
